# P1/P2/P4 weight-conversion item ranges re-split: P1 converts items 0..2047, P2 2048..17407, P4 17408..22527 (moves 1024 W2 items from the cross-attn phase into the attention phase background converter
# speedup vs baseline: 1.0016x; 1.0016x over previous
; #define LAS __attribute__((address_space(3)))
; __device__ __forceinline__ void cvt_fill_g(const Frame& F) { LAS float* gl = (LAS float*)(F.lds + BG_G_OFF); for (int i = F.tid; i < DM; i += NTHREADS) gl[i] = F.g_moe[i] * WSCALE; __syncthreads(); }
;     __device__ __forceinline__ void init(const Frame& F_, int first_item, int n_items) { init(F_, first_item, n_items, F_.vcu, F_.G); }
; __global__ void __launch_bounds__(NTHREADS, 2) mk_fwd(Args args) {
;     ...
;         if (F.G == 256 && blockIdx.x >= 208) {
;             cvt_fill_g(F);
;             Bg bg; bg.init(F, CVT_ITEMS - CVT_P9_ITEMS - CVT_P4_ITEMS - CVT_P1_ITEMS, CVT_P1_ITEMS, (int)blockIdx.x - 208, 48); bg.drain();
.LBB0_281:
	global_load_dword v6, v[2:3], off
	v_add_u32_e32 v5, 0x200, v5
	v_cmp_lt_u32_e32 vcc, s3, v5
	v_lshl_add_u64 v[2:3], v[2:3], 0, s[4:5]
	s_or_b64 s[0:1], vcc, s[0:1]
	s_waitcnt vmcnt(0)
	v_mul_f32_e32 v6, 0x42800000, v6
	ds_write_b32 v4, v6
	v_add_u32_e32 v4, 0x800, v4
	s_andn2_b64 exec, exec, s[0:1]
	s_cbranch_execnz .LBB0_281
	s_or_b64 exec, exec, s[0:1]
	v_readlane_b32 s1, v254, 8
	s_lshl_b32 s0, s2, 2
	s_lshr_b32 s1, s1, 7
	s_add_i32 s3, s0, s1
	s_addk_i32 s3, 0xfcc0
	s_cmpk_gt_i32 s3, 0x7ff
	s_cselect_b64 s[0:1], -1, 0
	s_mov_b32 s34, 0
	s_and_b64 vcc, exec, s[0:1]
	s_waitcnt lgkmcnt(0)
	s_barrier
	s_cbranch_vccnz .LBB0_284
	s_sub_i32 s4, 0x8bf, s3
	s_mul_hi_i32 s4, s4, 0x2aaaaaab
	s_lshr_b32 s5, s4, 31
	s_ashr_i32 s4, s4, 5
	s_add_i32 s4, s4, s5
	s_lshl_b32 s34, s4, 1

; #define LAS __attribute__((address_space(3)))
; __device__ __forceinline__ void cvt_fill_g(const Frame& F) { LAS float* gl = (LAS float*)(F.lds + BG_G_OFF); for (int i = F.tid; i < DM; i += NTHREADS) gl[i] = F.g_moe[i] * WSCALE; __syncthreads(); }
;     __device__ __forceinline__ void init(const Frame& F_, int first_item, int n_items) { init(F_, first_item, n_items, F_.vcu, F_.G); }
; __global__ void __launch_bounds__(NTHREADS, 2) mk_fwd(Args args) {
;     ...
;         cvt_fill_g(F);
;         Bg bg; bg.init(F, CVT_P0_ITEMS, CVT_ITEMS - CVT_P0_ITEMS - (F.G == 256 ? CVT_P9_ITEMS + CVT_P4_ITEMS + CVT_P1_ITEMS : 0));
.LBB0_367:
	global_load_dword v5, v[2:3], off
	v_add_u32_e32 v4, 0x200, v4
	v_cmp_lt_u32_e32 vcc, s3, v4
	v_lshl_add_u64 v[2:3], v[2:3], 0, s[4:5]
	s_or_b64 s[0:1], vcc, s[0:1]
	s_waitcnt vmcnt(0)
	v_mul_f32_e32 v5, 0x42800000, v5
	ds_write_b32 v1, v5
	v_add_u32_e32 v1, 0x800, v1
	s_andn2_b64 exec, exec, s[0:1]
	s_cbranch_execnz .LBB0_367
	s_or_b64 exec, exec, s[0:1]
	s_cmpk_eq_i32 s33, 0x100
	s_movk_i32 s0, 0x4400
	v_readlane_b32 s1, v254, 8
	s_cselect_b32 s0, s0, 0x6000
	s_lshl_b32 s3, s52, 2
	s_lshr_b32 s1, s1, 7
	s_add_i32 s3, s3, s1
	s_addk_i32 s3, 0x800
	s_lshl_b32 s55, s33, 2
	s_cmp_ge_i32 s3, s0
	s_mov_b32 s54, 0
	s_waitcnt lgkmcnt(0)
	s_barrier
	s_cbranch_scc1 .LBB0_370
	s_abs_i32 s1, s55
	v_cvt_f32_u32_e32 v1, s1
	s_add_i32 s0, s55, s0
	s_not_b32 s4, s3
	s_add_i32 s4, s4, s0
	v_rcp_iflag_f32_e32 v1, v1
	s_sub_i32 s0, 0, s1
	s_xor_b32 s5, s4, s55
	s_abs_i32 s4, s4
	v_mul_f32_e32 v1, 0x4f7ffffe, v1
	v_cvt_u32_f32_e32 v1, v1
	s_ashr_i32 s5, s5, 31
	v_readfirstlane_b32 s6, v1
	s_mul_i32 s0, s0, s6
	s_mul_hi_u32 s0, s6, s0
	s_add_i32 s6, s6, s0
	s_mul_hi_u32 s0, s4, s6
	s_mul_i32 s6, s0, s1
	s_sub_i32 s4, s4, s6
	s_add_i32 s7, s0, 1
	s_sub_i32 s6, s4, s1
	s_cmp_ge_u32 s4, s1
	s_cselect_b32 s0, s7, s0
	s_cselect_b32 s4, s6, s4
	s_add_i32 s6, s0, 1
	s_cmp_ge_u32 s4, s1
	s_cselect_b32 s0, s6, s0
	s_xor_b32 s0, s0, s5
	s_sub_i32 s0, s0, s5
	s_lshl_b32 s54, s0, 1

; #define LAS __attribute__((address_space(3)))
; __device__ __forceinline__ void cvt_fill_g(const Frame& F) { LAS float* gl = (LAS float*)(F.lds + BG_G_OFF); for (int i = F.tid; i < DM; i += NTHREADS) gl[i] = F.g_moe[i] * WSCALE; __syncthreads(); }
;     __device__ __forceinline__ void init(const Frame& F_, int first_item, int n_items) { init(F_, first_item, n_items, F_.vcu, F_.G); }
; __global__ void __launch_bounds__(NTHREADS, 2) mk_fwd(Args args) {
;     ...
;         if (F.G == 256 && blockIdx.x >= 128) {
;             cvt_fill_g(F);
;             Bg bg; bg.init(F, CVT_ITEMS - CVT_P9_ITEMS - CVT_P4_ITEMS, CVT_P4_ITEMS, (int)blockIdx.x - 128, 128); bg.drain();
.LBB0_892:
	global_load_dword v6, v[2:3], off
	v_add_u32_e32 v5, 0x200, v5
	v_cmp_lt_u32_e32 vcc, s3, v5
	v_lshl_add_u64 v[2:3], v[2:3], 0, s[4:5]
	s_or_b64 s[0:1], vcc, s[0:1]
	s_waitcnt vmcnt(0)
	v_mul_f32_e32 v6, 0x42800000, v6
	ds_write_b32 v4, v6
	v_add_u32_e32 v4, 0x800, v4
	s_andn2_b64 exec, exec, s[0:1]
	s_cbranch_execnz .LBB0_892
	s_or_b64 exec, exec, s[0:1]
	v_readlane_b32 s1, v254, 8
	s_lshl_b32 s0, s2, 2
	s_lshr_b32 s1, s1, 7
	s_add_i32 s3, s0, s1
	s_addk_i32 s3, 0x4200
	s_cmpk_gt_i32 s3, 0x57ff
	s_mov_b32 s34, 0
	s_waitcnt lgkmcnt(0)
	s_barrier
	s_cbranch_scc1 .LBB0_895
	s_sub_i32 s0, 0x59ff, s3
	s_ashr_i32 s1, s0, 31
	s_lshr_b32 s1, s1, 23
	s_add_i32 s0, s0, s1
	s_ashr_i32 s0, s0, 9
	s_lshl_b32 s34, s0, 1
